# speedup vs baseline: 1.0102x; 1.0102x over previous
.Lp_mask:
	s_sleep 32
	s_lshl_b32 s13, s13, 5
	v_lshl_add_u32 v20, v128, 2, s13
	v_lshlrev_b32_e32 v21, 12, v20
	v_lshl_add_u32 v21, v126, 4, v21
	v_add_u32_e32 v22, 0x1000, v21
	v_add_u32_e32 v23, 0x2000, v21
	v_add_u32_e32 v24, 0x3000, v21
	global_load_dwordx4 v[132:135], v21, s[34:35] nt
	global_load_dwordx4 v[136:139], v21, s[34:35] offset:1024 nt
	global_load_dwordx4 v[140:143], v21, s[34:35] offset:2048 nt
	global_load_dwordx4 v[144:147], v21, s[34:35] offset:3072 nt
	global_load_dwordx4 v[148:151], v22, s[34:35] nt
	global_load_dwordx4 v[152:155], v22, s[34:35] offset:1024 nt
	global_load_dwordx4 v[156:159], v22, s[34:35] offset:2048 nt
	global_load_dwordx4 v[160:163], v22, s[34:35] offset:3072 nt
	global_load_dwordx4 v[164:167], v23, s[34:35] nt
	global_load_dwordx4 v[168:171], v23, s[34:35] offset:1024 nt
	global_load_dwordx4 v[172:175], v23, s[34:35] offset:2048 nt
	global_load_dwordx4 v[176:179], v23, s[34:35] offset:3072 nt
	global_load_dwordx4 v[180:183], v24, s[34:35] nt
	global_load_dwordx4 v[184:187], v24, s[34:35] offset:1024 nt
	global_load_dwordx4 v[188:191], v24, s[34:35] offset:2048 nt
	global_load_dwordx4 v[192:195], v24, s[34:35] offset:3072 nt
	s_waitcnt vmcnt(12)
	v_mov_b32_e32 v44, 0
	v_cmp_ne_u32_e64 s[46:47], 0, v147
	v_cmp_ne_u32_e64 s[48:49], 0, v146
	v_cmp_ne_u32_e64 s[50:51], 0, v145
	v_cmp_ne_u32_e64 s[52:53], 0, v144
	v_addc_co_u32_e64 v44, s[54:55], v44, v44, s[46:47]
	v_addc_co_u32_e64 v44, s[54:55], v44, v44, s[48:49]
	v_addc_co_u32_e64 v44, s[54:55], v44, v44, s[50:51]
	v_addc_co_u32_e64 v44, s[54:55], v44, v44, s[52:53]
	v_cmp_ne_u32_e64 s[46:47], 0, v143
	v_cmp_ne_u32_e64 s[48:49], 0, v142
	v_cmp_ne_u32_e64 s[50:51], 0, v141
	v_cmp_ne_u32_e64 s[52:53], 0, v140
	v_addc_co_u32_e64 v44, s[54:55], v44, v44, s[46:47]
	v_addc_co_u32_e64 v44, s[54:55], v44, v44, s[48:49]
	v_addc_co_u32_e64 v44, s[54:55], v44, v44, s[50:51]
	v_addc_co_u32_e64 v44, s[54:55], v44, v44, s[52:53]
	v_cmp_ne_u32_e64 s[46:47], 0, v139
	v_cmp_ne_u32_e64 s[48:49], 0, v138
	v_cmp_ne_u32_e64 s[50:51], 0, v137
	v_cmp_ne_u32_e64 s[52:53], 0, v136
	v_addc_co_u32_e64 v44, s[54:55], v44, v44, s[46:47]
	v_addc_co_u32_e64 v44, s[54:55], v44, v44, s[48:49]
	v_addc_co_u32_e64 v44, s[54:55], v44, v44, s[50:51]
	v_addc_co_u32_e64 v44, s[54:55], v44, v44, s[52:53]
	v_cmp_ne_u32_e64 s[46:47], 0, v135
	v_cmp_ne_u32_e64 s[48:49], 0, v134
	v_cmp_ne_u32_e64 s[50:51], 0, v133
	v_cmp_ne_u32_e64 s[52:53], 0, v132
	v_addc_co_u32_e64 v44, s[54:55], v44, v44, s[46:47]
	v_addc_co_u32_e64 v44, s[54:55], v44, v44, s[48:49]
	v_addc_co_u32_e64 v44, s[54:55], v44, v44, s[50:51]
	v_addc_co_u32_e64 v44, s[54:55], v44, v44, s[52:53]
	s_waitcnt vmcnt(8)
	v_mov_b32_e32 v45, 0
	v_cmp_ne_u32_e64 s[46:47], 0, v163
	v_cmp_ne_u32_e64 s[48:49], 0, v162
	v_cmp_ne_u32_e64 s[50:51], 0, v161
	v_cmp_ne_u32_e64 s[52:53], 0, v160
	v_addc_co_u32_e64 v45, s[54:55], v45, v45, s[46:47]
	v_addc_co_u32_e64 v45, s[54:55], v45, v45, s[48:49]
	v_addc_co_u32_e64 v45, s[54:55], v45, v45, s[50:51]
	v_addc_co_u32_e64 v45, s[54:55], v45, v45, s[52:53]
	v_cmp_ne_u32_e64 s[46:47], 0, v159
	v_cmp_ne_u32_e64 s[48:49], 0, v158
	v_cmp_ne_u32_e64 s[50:51], 0, v157
	v_cmp_ne_u32_e64 s[52:53], 0, v156
	v_addc_co_u32_e64 v45, s[54:55], v45, v45, s[46:47]
	v_addc_co_u32_e64 v45, s[54:55], v45, v45, s[48:49]
	v_addc_co_u32_e64 v45, s[54:55], v45, v45, s[50:51]
	v_addc_co_u32_e64 v45, s[54:55], v45, v45, s[52:53]
	v_cmp_ne_u32_e64 s[46:47], 0, v155
	v_cmp_ne_u32_e64 s[48:49], 0, v154
	v_cmp_ne_u32_e64 s[50:51], 0, v153
	v_cmp_ne_u32_e64 s[52:53], 0, v152
	v_addc_co_u32_e64 v45, s[54:55], v45, v45, s[46:47]
	v_addc_co_u32_e64 v45, s[54:55], v45, v45, s[48:49]
	v_addc_co_u32_e64 v45, s[54:55], v45, v45, s[50:51]
	v_addc_co_u32_e64 v45, s[54:55], v45, v45, s[52:53]
	v_cmp_ne_u32_e64 s[46:47], 0, v151
	v_cmp_ne_u32_e64 s[48:49], 0, v150
	v_cmp_ne_u32_e64 s[50:51], 0, v149
	v_cmp_ne_u32_e64 s[52:53], 0, v148
	v_addc_co_u32_e64 v45, s[54:55], v45, v45, s[46:47]
	v_addc_co_u32_e64 v45, s[54:55], v45, v45, s[48:49]
	v_addc_co_u32_e64 v45, s[54:55], v45, v45, s[50:51]
	v_addc_co_u32_e64 v45, s[54:55], v45, v45, s[52:53]
	s_waitcnt vmcnt(4)
	v_mov_b32_e32 v46, 0
	v_cmp_ne_u32_e64 s[46:47], 0, v179
	v_cmp_ne_u32_e64 s[48:49], 0, v178
	v_cmp_ne_u32_e64 s[50:51], 0, v177
	v_cmp_ne_u32_e64 s[52:53], 0, v176
	v_addc_co_u32_e64 v46, s[54:55], v46, v46, s[46:47]
	v_addc_co_u32_e64 v46, s[54:55], v46, v46, s[48:49]
	v_addc_co_u32_e64 v46, s[54:55], v46, v46, s[50:51]
	v_addc_co_u32_e64 v46, s[54:55], v46, v46, s[52:53]
	v_cmp_ne_u32_e64 s[46:47], 0, v175
	v_cmp_ne_u32_e64 s[48:49], 0, v174
	v_cmp_ne_u32_e64 s[50:51], 0, v173
	v_cmp_ne_u32_e64 s[52:53], 0, v172
	v_addc_co_u32_e64 v46, s[54:55], v46, v46, s[46:47]
	v_addc_co_u32_e64 v46, s[54:55], v46, v46, s[48:49]
	v_addc_co_u32_e64 v46, s[54:55], v46, v46, s[50:51]
	v_addc_co_u32_e64 v46, s[54:55], v46, v46, s[52:53]
	v_cmp_ne_u32_e64 s[46:47], 0, v171
	v_cmp_ne_u32_e64 s[48:49], 0, v170
	v_cmp_ne_u32_e64 s[50:51], 0, v169
	v_cmp_ne_u32_e64 s[52:53], 0, v168
	v_addc_co_u32_e64 v46, s[54:55], v46, v46, s[46:47]
	v_addc_co_u32_e64 v46, s[54:55], v46, v46, s[48:49]
	v_addc_co_u32_e64 v46, s[54:55], v46, v46, s[50:51]
	v_addc_co_u32_e64 v46, s[54:55], v46, v46, s[52:53]
	v_cmp_ne_u32_e64 s[46:47], 0, v167
	v_cmp_ne_u32_e64 s[48:49], 0, v166
	v_cmp_ne_u32_e64 s[50:51], 0, v165
	v_cmp_ne_u32_e64 s[52:53], 0, v164
	v_addc_co_u32_e64 v46, s[54:55], v46, v46, s[46:47]
	v_addc_co_u32_e64 v46, s[54:55], v46, v46, s[48:49]
	v_addc_co_u32_e64 v46, s[54:55], v46, v46, s[50:51]
	v_addc_co_u32_e64 v46, s[54:55], v46, v46, s[52:53]
	s_waitcnt vmcnt(0)
	v_mov_b32_e32 v47, 0
	v_cmp_ne_u32_e64 s[46:47], 0, v195
	v_cmp_ne_u32_e64 s[48:49], 0, v194
	v_cmp_ne_u32_e64 s[50:51], 0, v193
	v_cmp_ne_u32_e64 s[52:53], 0, v192
	v_addc_co_u32_e64 v47, s[54:55], v47, v47, s[46:47]
	v_addc_co_u32_e64 v47, s[54:55], v47, v47, s[48:49]
	v_addc_co_u32_e64 v47, s[54:55], v47, v47, s[50:51]
	v_addc_co_u32_e64 v47, s[54:55], v47, v47, s[52:53]
	v_cmp_ne_u32_e64 s[46:47], 0, v191
	v_cmp_ne_u32_e64 s[48:49], 0, v190
	v_cmp_ne_u32_e64 s[50:51], 0, v189
	v_cmp_ne_u32_e64 s[52:53], 0, v188
	v_addc_co_u32_e64 v47, s[54:55], v47, v47, s[46:47]
	v_addc_co_u32_e64 v47, s[54:55], v47, v47, s[48:49]
	v_addc_co_u32_e64 v47, s[54:55], v47, v47, s[50:51]
	v_addc_co_u32_e64 v47, s[54:55], v47, v47, s[52:53]
	v_cmp_ne_u32_e64 s[46:47], 0, v187
	v_cmp_ne_u32_e64 s[48:49], 0, v186
	v_cmp_ne_u32_e64 s[50:51], 0, v185
	v_cmp_ne_u32_e64 s[52:53], 0, v184
	v_addc_co_u32_e64 v47, s[54:55], v47, v47, s[46:47]
	v_addc_co_u32_e64 v47, s[54:55], v47, v47, s[48:49]
	v_addc_co_u32_e64 v47, s[54:55], v47, v47, s[50:51]
	v_addc_co_u32_e64 v47, s[54:55], v47, v47, s[52:53]
	v_cmp_ne_u32_e64 s[46:47], 0, v183
	v_cmp_ne_u32_e64 s[48:49], 0, v182
	v_cmp_ne_u32_e64 s[50:51], 0, v181
	v_cmp_ne_u32_e64 s[52:53], 0, v180
	v_addc_co_u32_e64 v47, s[54:55], v47, v47, s[46:47]
	v_addc_co_u32_e64 v47, s[54:55], v47, v47, s[48:49]
	v_addc_co_u32_e64 v47, s[54:55], v47, v47, s[50:51]
	v_addc_co_u32_e64 v47, s[54:55], v47, v47, s[52:53]
	v_lshlrev_b32_e32 v28, 7, v20
	v_lshl_add_u32 v28, v126, 1, v28
	global_store_short v28, v44, s[36:37] sc1
	global_store_short v28, v45, s[36:37] offset:128 sc1
	global_store_short v28, v46, s[36:37] offset:256 sc1
	global_store_short v28, v47, s[36:37] offset:384 sc1
	s_endpgm
